# v59 + nt on the short-conv input loads (read once)
# baseline (speedup 1.0000x reference)
.LBB0_1175:
	s_or_b64 exec, exec, s[16:17]
	v_lshlrev_b64 v[28:29], 9, v[98:99]
	v_lshl_add_u64 v[102:103], v[28:29], 1, v[96:97]
	global_load_dwordx4 v[82:85], v[26:27], off nt
	global_load_dwordx4 v[110:113], v[102:103], off nt
	global_load_dwordx4 v[74:77], v[26:27], off offset:1024 nt
	global_load_dwordx4 v[78:81], v[102:103], off offset:1024 nt
	global_load_dwordx4 v[66:69], v[26:27], off offset:2048 nt
	global_load_dwordx4 v[70:73], v[102:103], off offset:2048 nt
	global_load_dwordx4 v[58:61], v[26:27], off offset:3072 nt
	global_load_dwordx4 v[62:65], v[102:103], off offset:3072 nt
	s_movk_i32 s16, 0x1000
	v_add_co_u32_e32 v26, vcc, s16, v26
	s_waitcnt vmcnt(8)
	v_lshlrev_b32_e32 v114, 16, v90
	v_addc_co_u32_e32 v27, vcc, 0, v27, vcc
	global_load_dwordx4 v[50:53], v[26:27], off nt
	v_add_co_u32_e32 v100, vcc, s16, v102
	v_and_b32_e32 v115, 0xffff0000, v90
	s_nop 0
	v_addc_co_u32_e32 v101, vcc, 0, v103, vcc
	global_load_dwordx4 v[54:57], v[100:101], off nt
	global_load_dwordx4 v[42:45], v[26:27], off offset:1024 nt
	global_load_dwordx4 v[46:49], v[100:101], off offset:1024 nt
	global_load_dwordx4 v[34:37], v[26:27], off offset:2048 nt
	global_load_dwordx4 v[38:41], v[100:101], off offset:2048 nt
	s_nop 0
	global_load_dwordx4 v[26:29], v[26:27], off offset:3072 nt
	s_nop 0
	global_load_dwordx4 v[30:33], v[100:101], off offset:3072 nt
	v_lshlrev_b32_e32 v104, 16, v86
	v_and_b32_e32 v105, 0xffff0000, v86
	v_pk_mul_f32 v[116:117], v[10:11], v[114:115]
	v_lshlrev_b32_e32 v90, 16, v91
	v_pk_fma_f32 v[116:117], v[18:19], v[104:105], v[116:117]
	v_and_b32_e32 v91, 0xffff0000, v91
	v_lshlrev_b32_e32 v86, 16, v87
	v_and_b32_e32 v87, 0xffff0000, v87
	v_readlane_b32 s16, v253, 8
	v_add_u32_e32 v108, s72, v108
	s_waitcnt vmcnt(15)
	v_lshlrev_b32_e32 v104, 16, v82
	v_and_b32_e32 v105, 0xffff0000, v82
	s_waitcnt vmcnt(14)
	v_lshlrev_b32_e32 v106, 16, v110
	v_and_b32_e32 v107, 0xffff0000, v110
	v_pk_fma_f32 v[116:117], v[2:3], v[104:105], v[116:117]
	v_lshlrev_b32_e32 v82, 16, v83
	v_pk_mul_f32 v[116:117], v[116:117], v[106:107]
	v_lshlrev_b32_e32 v106, 16, v111
	v_and_b32_e32 v107, 0xffff0000, v111
	v_pk_mul_f32 v[110:111], v[12:13], v[90:91]
	v_and_b32_e32 v83, 0xffff0000, v83
	v_pk_fma_f32 v[86:87], v[20:21], v[86:87], v[110:111]
	v_lshlrev_b32_e32 v110, 16, v112
	v_pk_fma_f32 v[86:87], v[4:5], v[82:83], v[86:87]
	v_and_b32_e32 v111, 0xffff0000, v112
	v_pk_mul_f32 v[118:119], v[86:87], v[106:107]
	v_lshlrev_b32_e32 v106, 16, v92
	v_and_b32_e32 v107, 0xffff0000, v92
	v_lshlrev_b32_e32 v86, 16, v88
	v_and_b32_e32 v87, 0xffff0000, v88
	v_pk_mul_f32 v[120:121], v[14:15], v[106:107]
	v_lshlrev_b32_e32 v92, 16, v93
	v_pk_fma_f32 v[120:121], v[22:23], v[86:87], v[120:121]
	v_lshlrev_b32_e32 v86, 16, v84
	v_and_b32_e32 v87, 0xffff0000, v84
	v_pk_fma_f32 v[120:121], v[6:7], v[86:87], v[120:121]
	v_and_b32_e32 v93, 0xffff0000, v93
	v_pk_mul_f32 v[120:121], v[120:121], v[110:111]
	v_lshlrev_b32_e32 v110, 16, v113
	v_and_b32_e32 v111, 0xffff0000, v113
	v_lshlrev_b32_e32 v88, 16, v89
	v_and_b32_e32 v89, 0xffff0000, v89
	v_pk_mul_f32 v[112:113], v[16:17], v[92:93]
	v_lshlrev_b32_e32 v84, 16, v85
	v_pk_fma_f32 v[88:89], v[24:25], v[88:89], v[112:113]
	v_and_b32_e32 v85, 0xffff0000, v85
	v_pk_fma_f32 v[88:89], v[8:9], v[84:85], v[88:89]
	v_cvt_pk_bf16_f32 v112, v120, v121
	v_pk_mul_f32 v[88:89], v[88:89], v[110:111]
	v_cvt_pk_bf16_f32 v110, v116, v117
	v_cvt_pk_bf16_f32 v111, v118, v119
	v_cvt_pk_bf16_f32 v113, v88, v89
	global_store_dwordx4 v[102:103], v[110:113], off sc1
	s_waitcnt vmcnt(13)
	v_lshlrev_b32_e32 v88, 16, v78
	v_and_b32_e32 v89, 0xffff0000, v78
	v_pk_mul_f32 v[110:111], v[10:11], v[104:105]
	v_lshlrev_b32_e32 v112, 16, v74
	v_pk_fma_f32 v[110:111], v[18:19], v[114:115], v[110:111]
	v_and_b32_e32 v113, 0xffff0000, v74
	v_pk_fma_f32 v[110:111], v[2:3], v[112:113], v[110:111]
	v_lshlrev_b32_e32 v78, 16, v79
	v_pk_mul_f32 v[88:89], v[110:111], v[88:89]
	v_pk_mul_f32 v[110:111], v[12:13], v[82:83]
	v_and_b32_e32 v79, 0xffff0000, v79
	v_pk_fma_f32 v[90:91], v[20:21], v[90:91], v[110:111]
	v_lshlrev_b32_e32 v110, 16, v75
	v_and_b32_e32 v111, 0xffff0000, v75
	v_pk_fma_f32 v[74:75], v[4:5], v[110:111], v[90:91]
	v_pk_mul_f32 v[90:91], v[14:15], v[86:87]
	v_pk_mul_f32 v[78:79], v[74:75], v[78:79]
	v_pk_fma_f32 v[90:91], v[22:23], v[106:107], v[90:91]
	v_lshlrev_b32_e32 v106, 16, v76
	v_and_b32_e32 v107, 0xffff0000, v76
	v_lshlrev_b32_e32 v74, 16, v80
	v_and_b32_e32 v75, 0xffff0000, v80
	v_pk_fma_f32 v[90:91], v[6:7], v[106:107], v[90:91]
	v_add_u32_e32 v98, s16, v98
	v_pk_mul_f32 v[90:91], v[90:91], v[74:75]
	v_lshlrev_b32_e32 v74, 16, v81
	v_and_b32_e32 v75, 0xffff0000, v81
	v_pk_mul_f32 v[80:81], v[16:17], v[84:85]
	s_movk_i32 s16, 0x7ff
	v_pk_fma_f32 v[80:81], v[24:25], v[92:93], v[80:81]
	v_lshlrev_b32_e32 v92, 16, v77
	v_and_b32_e32 v93, 0xffff0000, v77
	v_pk_fma_f32 v[76:77], v[8:9], v[92:93], v[80:81]
	v_cmp_lt_i32_e32 vcc, s16, v108
	v_pk_mul_f32 v[80:81], v[76:77], v[74:75]
	v_cvt_pk_bf16_f32 v74, v88, v89
	v_cvt_pk_bf16_f32 v75, v78, v79
	v_cvt_pk_bf16_f32 v76, v90, v91
	v_cvt_pk_bf16_f32 v77, v80, v81
	global_store_dwordx4 v[102:103], v[74:77], off offset:1024 sc1
	s_waitcnt vmcnt(13)
	v_lshlrev_b32_e32 v78, 16, v66
	v_and_b32_e32 v79, 0xffff0000, v66
	v_pk_mul_f32 v[76:77], v[10:11], v[112:113]
	s_waitcnt vmcnt(12)
	v_lshlrev_b32_e32 v74, 16, v70
	v_pk_fma_f32 v[76:77], v[18:19], v[104:105], v[76:77]
	v_and_b32_e32 v75, 0xffff0000, v70
	v_pk_fma_f32 v[76:77], v[2:3], v[78:79], v[76:77]
	v_lshlrev_b32_e32 v80, 16, v67
	v_pk_mul_f32 v[74:75], v[76:77], v[74:75]
	v_pk_mul_f32 v[76:77], v[12:13], v[110:111]
	v_and_b32_e32 v81, 0xffff0000, v67
	v_pk_fma_f32 v[76:77], v[20:21], v[82:83], v[76:77]
	v_lshlrev_b32_e32 v70, 16, v71
	v_pk_fma_f32 v[66:67], v[4:5], v[80:81], v[76:77]
	v_pk_mul_f32 v[76:77], v[14:15], v[106:107]
	v_and_b32_e32 v71, 0xffff0000, v71
	v_pk_fma_f32 v[76:77], v[22:23], v[86:87], v[76:77]
	v_lshlrev_b32_e32 v82, 16, v68
	v_and_b32_e32 v83, 0xffff0000, v68
	v_pk_mul_f32 v[70:71], v[66:67], v[70:71]
	v_lshlrev_b32_e32 v66, 16, v72
	v_and_b32_e32 v67, 0xffff0000, v72
	v_pk_fma_f32 v[76:77], v[6:7], v[82:83], v[76:77]
	s_or_b64 s[14:15], vcc, s[14:15]
	v_pk_mul_f32 v[76:77], v[76:77], v[66:67]
	v_lshlrev_b32_e32 v66, 16, v73
	v_and_b32_e32 v67, 0xffff0000, v73
	v_pk_mul_f32 v[72:73], v[16:17], v[92:93]
	s_nop 0
	v_pk_fma_f32 v[72:73], v[24:25], v[84:85], v[72:73]
	v_lshlrev_b32_e32 v84, 16, v69
	v_and_b32_e32 v85, 0xffff0000, v69
	v_pk_fma_f32 v[68:69], v[8:9], v[84:85], v[72:73]
	s_nop 0
	v_pk_mul_f32 v[72:73], v[68:69], v[66:67]
	v_cvt_pk_bf16_f32 v66, v74, v75
	v_cvt_pk_bf16_f32 v67, v70, v71
	v_cvt_pk_bf16_f32 v68, v76, v77
	v_cvt_pk_bf16_f32 v69, v72, v73
	global_store_dwordx4 v[102:103], v[66:69], off offset:2048 sc1
	s_waitcnt vmcnt(12)
	v_lshlrev_b32_e32 v70, 16, v58
	v_and_b32_e32 v71, 0xffff0000, v58
	v_pk_mul_f32 v[68:69], v[10:11], v[78:79]
	s_waitcnt vmcnt(11)
	v_lshlrev_b32_e32 v66, 16, v62
	v_pk_fma_f32 v[68:69], v[18:19], v[112:113], v[68:69]
	v_and_b32_e32 v67, 0xffff0000, v62
	v_pk_fma_f32 v[68:69], v[2:3], v[70:71], v[68:69]
	v_lshlrev_b32_e32 v72, 16, v59
	v_pk_mul_f32 v[66:67], v[68:69], v[66:67]
	v_pk_mul_f32 v[68:69], v[12:13], v[80:81]
	v_and_b32_e32 v73, 0xffff0000, v59
	v_pk_fma_f32 v[68:69], v[20:21], v[110:111], v[68:69]
	v_lshlrev_b32_e32 v62, 16, v63
	v_pk_fma_f32 v[58:59], v[4:5], v[72:73], v[68:69]
	v_pk_mul_f32 v[68:69], v[14:15], v[82:83]
	v_and_b32_e32 v63, 0xffff0000, v63
	v_pk_fma_f32 v[68:69], v[22:23], v[106:107], v[68:69]
	v_lshlrev_b32_e32 v74, 16, v60
	v_and_b32_e32 v75, 0xffff0000, v60
	v_pk_mul_f32 v[62:63], v[58:59], v[62:63]
	v_lshlrev_b32_e32 v58, 16, v64
	v_and_b32_e32 v59, 0xffff0000, v64
	v_pk_fma_f32 v[68:69], v[6:7], v[74:75], v[68:69]
	v_lshlrev_b32_e32 v76, 16, v61
	v_pk_mul_f32 v[68:69], v[68:69], v[58:59]
	v_lshlrev_b32_e32 v58, 16, v65
	v_and_b32_e32 v59, 0xffff0000, v65
	v_pk_mul_f32 v[64:65], v[16:17], v[84:85]
	v_and_b32_e32 v77, 0xffff0000, v61
	v_pk_fma_f32 v[64:65], v[24:25], v[92:93], v[64:65]
	s_nop 0
	v_pk_fma_f32 v[60:61], v[8:9], v[76:77], v[64:65]
	s_nop 0
	v_pk_mul_f32 v[64:65], v[60:61], v[58:59]
	v_cvt_pk_bf16_f32 v58, v66, v67
	v_cvt_pk_bf16_f32 v59, v62, v63
	v_cvt_pk_bf16_f32 v60, v68, v69
	v_cvt_pk_bf16_f32 v61, v64, v65
	global_store_dwordx4 v[102:103], v[58:61], off offset:3072 sc1
	s_waitcnt vmcnt(11)
	v_lshlrev_b32_e32 v62, 16, v50
	v_and_b32_e32 v63, 0xffff0000, v50
	v_pk_mul_f32 v[60:61], v[10:11], v[70:71]
	s_waitcnt vmcnt(10)
	v_lshlrev_b32_e32 v58, 16, v54
	v_pk_fma_f32 v[60:61], v[18:19], v[78:79], v[60:61]
	v_and_b32_e32 v59, 0xffff0000, v54
	v_pk_fma_f32 v[60:61], v[2:3], v[62:63], v[60:61]
	v_lshlrev_b32_e32 v64, 16, v51
	v_pk_mul_f32 v[58:59], v[60:61], v[58:59]
	v_pk_mul_f32 v[60:61], v[12:13], v[72:73]
	v_and_b32_e32 v65, 0xffff0000, v51
	v_pk_fma_f32 v[60:61], v[20:21], v[80:81], v[60:61]
	v_lshlrev_b32_e32 v54, 16, v55
	v_pk_fma_f32 v[50:51], v[4:5], v[64:65], v[60:61]
	v_pk_mul_f32 v[60:61], v[14:15], v[74:75]
	v_and_b32_e32 v55, 0xffff0000, v55
	v_pk_fma_f32 v[60:61], v[22:23], v[82:83], v[60:61]
	v_lshlrev_b32_e32 v66, 16, v52
	v_and_b32_e32 v67, 0xffff0000, v52
	v_pk_mul_f32 v[54:55], v[50:51], v[54:55]
	v_lshlrev_b32_e32 v50, 16, v56
	v_and_b32_e32 v51, 0xffff0000, v56
	v_pk_fma_f32 v[60:61], v[6:7], v[66:67], v[60:61]
	v_lshlrev_b32_e32 v68, 16, v53
	v_pk_mul_f32 v[60:61], v[60:61], v[50:51]
	v_lshlrev_b32_e32 v50, 16, v57
	v_and_b32_e32 v51, 0xffff0000, v57
	v_pk_mul_f32 v[56:57], v[16:17], v[76:77]
	v_and_b32_e32 v69, 0xffff0000, v53
	v_pk_fma_f32 v[56:57], v[24:25], v[84:85], v[56:57]
	s_nop 0
	v_pk_fma_f32 v[52:53], v[8:9], v[68:69], v[56:57]
	s_nop 0
	v_pk_mul_f32 v[56:57], v[52:53], v[50:51]
	v_cvt_pk_bf16_f32 v50, v58, v59
	v_cvt_pk_bf16_f32 v51, v54, v55
	v_cvt_pk_bf16_f32 v52, v60, v61
	v_cvt_pk_bf16_f32 v53, v56, v57
	global_store_dwordx4 v[100:101], v[50:53], off sc1
	s_waitcnt vmcnt(10)
	v_lshlrev_b32_e32 v54, 16, v42
	v_and_b32_e32 v55, 0xffff0000, v42
	v_pk_mul_f32 v[52:53], v[10:11], v[62:63]
	s_waitcnt vmcnt(9)
	v_lshlrev_b32_e32 v50, 16, v46
	v_pk_fma_f32 v[52:53], v[18:19], v[70:71], v[52:53]
	v_and_b32_e32 v51, 0xffff0000, v46
	v_pk_fma_f32 v[52:53], v[2:3], v[54:55], v[52:53]
	v_lshlrev_b32_e32 v56, 16, v43
	v_pk_mul_f32 v[50:51], v[52:53], v[50:51]
	v_pk_mul_f32 v[52:53], v[12:13], v[64:65]
	v_and_b32_e32 v57, 0xffff0000, v43
	v_pk_fma_f32 v[52:53], v[20:21], v[72:73], v[52:53]
	v_lshlrev_b32_e32 v46, 16, v47
	v_pk_fma_f32 v[42:43], v[4:5], v[56:57], v[52:53]
	v_pk_mul_f32 v[52:53], v[14:15], v[66:67]
	v_and_b32_e32 v47, 0xffff0000, v47
	v_pk_fma_f32 v[52:53], v[22:23], v[74:75], v[52:53]
	v_lshlrev_b32_e32 v58, 16, v44
	v_and_b32_e32 v59, 0xffff0000, v44
	v_pk_mul_f32 v[46:47], v[42:43], v[46:47]
	v_lshlrev_b32_e32 v42, 16, v48
	v_and_b32_e32 v43, 0xffff0000, v48
	v_pk_fma_f32 v[52:53], v[6:7], v[58:59], v[52:53]
	v_lshlrev_b32_e32 v60, 16, v45
	v_pk_mul_f32 v[52:53], v[52:53], v[42:43]
	v_lshlrev_b32_e32 v42, 16, v49
	v_and_b32_e32 v43, 0xffff0000, v49
	v_pk_mul_f32 v[48:49], v[16:17], v[68:69]
	v_and_b32_e32 v61, 0xffff0000, v45
	v_pk_fma_f32 v[48:49], v[24:25], v[76:77], v[48:49]
	s_nop 0
	v_pk_fma_f32 v[44:45], v[8:9], v[60:61], v[48:49]
	s_nop 0
	v_pk_mul_f32 v[48:49], v[44:45], v[42:43]
	v_cvt_pk_bf16_f32 v42, v50, v51
	v_cvt_pk_bf16_f32 v43, v46, v47
	v_cvt_pk_bf16_f32 v44, v52, v53
	v_cvt_pk_bf16_f32 v45, v48, v49
	global_store_dwordx4 v[100:101], v[42:45], off offset:1024 sc1
	s_waitcnt vmcnt(9)
	v_lshlrev_b32_e32 v46, 16, v34
	v_and_b32_e32 v47, 0xffff0000, v34
	v_pk_mul_f32 v[44:45], v[10:11], v[54:55]
	s_waitcnt vmcnt(8)
	v_lshlrev_b32_e32 v42, 16, v38
	v_pk_fma_f32 v[44:45], v[18:19], v[62:63], v[44:45]
	v_and_b32_e32 v43, 0xffff0000, v38
	v_pk_fma_f32 v[44:45], v[2:3], v[46:47], v[44:45]
	v_lshlrev_b32_e32 v48, 16, v35
	v_pk_mul_f32 v[42:43], v[44:45], v[42:43]
	v_pk_mul_f32 v[44:45], v[12:13], v[56:57]
	v_and_b32_e32 v49, 0xffff0000, v35
	v_pk_fma_f32 v[44:45], v[20:21], v[64:65], v[44:45]
	v_lshlrev_b32_e32 v38, 16, v39
	v_pk_fma_f32 v[34:35], v[4:5], v[48:49], v[44:45]
	v_pk_mul_f32 v[44:45], v[14:15], v[58:59]
	v_and_b32_e32 v39, 0xffff0000, v39
	v_pk_fma_f32 v[44:45], v[22:23], v[66:67], v[44:45]
	v_lshlrev_b32_e32 v50, 16, v36
	v_and_b32_e32 v51, 0xffff0000, v36
	v_pk_mul_f32 v[38:39], v[34:35], v[38:39]
	v_lshlrev_b32_e32 v34, 16, v40
	v_and_b32_e32 v35, 0xffff0000, v40
	v_pk_fma_f32 v[44:45], v[6:7], v[50:51], v[44:45]
	v_lshlrev_b32_e32 v52, 16, v37
	v_pk_mul_f32 v[44:45], v[44:45], v[34:35]
	v_lshlrev_b32_e32 v34, 16, v41
	v_and_b32_e32 v35, 0xffff0000, v41
	v_pk_mul_f32 v[40:41], v[16:17], v[60:61]
	v_and_b32_e32 v53, 0xffff0000, v37
	v_pk_fma_f32 v[40:41], v[24:25], v[68:69], v[40:41]
	s_nop 0
	v_pk_fma_f32 v[36:37], v[8:9], v[52:53], v[40:41]
	s_nop 0
	v_pk_mul_f32 v[40:41], v[36:37], v[34:35]
	v_cvt_pk_bf16_f32 v34, v42, v43
	v_cvt_pk_bf16_f32 v35, v38, v39
	v_cvt_pk_bf16_f32 v36, v44, v45
	v_cvt_pk_bf16_f32 v37, v40, v41
	global_store_dwordx4 v[100:101], v[34:37], off offset:2048 sc1
	s_waitcnt vmcnt(8)
	v_lshlrev_b32_e32 v38, 16, v26
	v_and_b32_e32 v39, 0xffff0000, v26
	v_pk_mul_f32 v[36:37], v[10:11], v[46:47]
	s_waitcnt vmcnt(7)
	v_lshlrev_b32_e32 v34, 16, v30
	v_pk_fma_f32 v[36:37], v[18:19], v[54:55], v[36:37]
	v_and_b32_e32 v35, 0xffff0000, v30
	v_pk_fma_f32 v[36:37], v[2:3], v[38:39], v[36:37]
	v_lshlrev_b32_e32 v26, 16, v27
	v_pk_mul_f32 v[34:35], v[36:37], v[34:35]
	v_pk_mul_f32 v[36:37], v[12:13], v[48:49]
	v_and_b32_e32 v27, 0xffff0000, v27
	v_pk_fma_f32 v[36:37], v[20:21], v[56:57], v[36:37]
	v_lshlrev_b32_e32 v30, 16, v31
	v_pk_fma_f32 v[26:27], v[4:5], v[26:27], v[36:37]
	v_pk_mul_f32 v[36:37], v[14:15], v[50:51]
	v_and_b32_e32 v31, 0xffff0000, v31
	v_pk_fma_f32 v[36:37], v[22:23], v[58:59], v[36:37]
	v_lshlrev_b32_e32 v38, 16, v28
	v_and_b32_e32 v39, 0xffff0000, v28
	v_pk_mul_f32 v[30:31], v[26:27], v[30:31]
	v_lshlrev_b32_e32 v26, 16, v32
	v_and_b32_e32 v27, 0xffff0000, v32
	v_pk_fma_f32 v[36:37], v[6:7], v[38:39], v[36:37]
	v_lshlrev_b32_e32 v28, 16, v29
	v_pk_mul_f32 v[36:37], v[36:37], v[26:27]
	v_lshlrev_b32_e32 v26, 16, v33
	v_and_b32_e32 v27, 0xffff0000, v33
	v_pk_mul_f32 v[32:33], v[16:17], v[52:53]
	v_and_b32_e32 v29, 0xffff0000, v29
	v_pk_fma_f32 v[32:33], v[24:25], v[60:61], v[32:33]
	s_nop 0
	v_pk_fma_f32 v[28:29], v[8:9], v[28:29], v[32:33]
	s_nop 0
	v_pk_mul_f32 v[32:33], v[28:29], v[26:27]
	v_cvt_pk_bf16_f32 v26, v34, v35
	v_cvt_pk_bf16_f32 v27, v30, v31
	v_cvt_pk_bf16_f32 v28, v36, v37
	v_cvt_pk_bf16_f32 v29, v32, v33
	global_store_dwordx4 v[100:101], v[26:29], off offset:3072 sc1
	s_andn2_b64 exec, exec, s[14:15]
	s_cbranch_execz .LBB0_1178
.LBB0_1176:
	v_ashrrev_i32_e32 v99, 31, v98
	v_and_b32_e32 v0, 0x3ff, v108
	v_lshlrev_b64 v[26:27], 10, v[98:99]
	v_mov_b32_e32 v86, 0
	v_cmp_ne_u32_e32 vcc, 0, v0
	v_lshl_add_u64 v[26:27], v[94:95], 0, v[26:27]
	v_mov_b32_e32 v87, 0
	v_mov_b32_e32 v88, 0
	v_mov_b32_e32 v89, 0
	v_mov_b32_e32 v90, 0
	v_mov_b32_e32 v91, 0
	v_mov_b32_e32 v92, 0
	v_mov_b32_e32 v93, 0
	s_and_saveexec_b64 s[16:17], vcc
	s_cbranch_execz .LBB0_1175
	global_load_dwordx4 v[86:89], v[26:27], off offset:-2048 nt
	global_load_dwordx4 v[90:93], v[26:27], off offset:-1024 nt
	s_branch .LBB0_1175
